# v45_touch3
# speedup vs baseline: 1.0116x; 1.0116x over previous
_Z10k_enc_scanPKDF16_PKfS2_S2_S2_S2_S2_S2_S2_S2_S2_S0_S2_S2_S2_S2_S2_S0_S2_PfPjS2_S2_S2_S2_S2_S2_S2_S2_S2_S2_S2_S2_PDF16_S5_S3_:
	s_load_dwordx4 s[52:55], s[0:1], 0x98
	s_cmp_gt_u32 s2, 15
	s_mov_b64 s[4:5], -1
	s_cbranch_scc0 .LBB3_39
	s_add_i32 s3, s2, -16
	s_cmpk_gt_i32 s3, 0x33f
	s_cbranch_scc1 .LBB3_38
	v_add_u32_e32 v5, 0x140, v0
	v_add_u32_e32 v6, 0x280, v0
	v_mul_u32_u24_e32 v3, 0x5f5, v5
	v_add_u32_e32 v7, 0x3c0, v0
	v_lshrrev_b32_e32 v10, 17, v3
	v_mul_u32_u24_e32 v3, 0xbe9, v6
	v_add_u32_e32 v8, 0x500, v0
	v_lshrrev_b32_e32 v11, 18, v3
	v_mul_u32_u24_e32 v3, 0xbe9, v7
	v_add_u32_e32 v2, 0x640, v0
	v_lshrrev_b32_e32 v12, 18, v3
	v_mul_u32_u24_e32 v3, 0xbe9, v8
	s_load_dwordx2 s[20:21], s[0:1], 0x90
	s_load_dwordx4 s[56:59], s[0:1], 0x80
	s_load_dwordx8 s[12:19], s[0:1], 0x60
	s_load_dwordx8 s[24:31], s[0:1], 0x40
	s_load_dwordx8 s[36:43], s[0:1], 0x0
	s_load_dwordx8 s[44:51], s[0:1], 0x20
	v_lshrrev_b32_e32 v14, 18, v3
	v_mul_u32_u24_e32 v3, 0x17d1, v2
	s_movk_i32 s4, 0xffaa
	v_lshrrev_b32_e32 v16, 19, v3
	v_mad_i32_i24 v116, v16, s4, v2
	v_mul_u32_u24_e32 v2, 22, v0
	v_mov_b32_e32 v67, 0
	v_lshlrev_b32_e32 v66, 2, v2
	v_mul_u32_u24_e32 v2, 11, v0
	s_waitcnt lgkmcnt(0)
	v_lshl_add_u64 v[72:73], s[40:41], 0, v[66:67]
	v_lshlrev_b32_e32 v66, 2, v2
	v_lshrrev_b32_e32 v2, 1, v0
	v_lshl_add_u64 v[76:77], s[44:45], 0, v[66:67]
	v_and_b32_e32 v117, 0xfc, v2
	v_and_b32_e32 v2, 0x1c0, v0
	s_movk_i32 s8, 0xc0
	v_add_u32_e32 v66, 0xffffff40, v0
	v_cmp_eq_u32_e64 s[8:9], s8, v2
	v_lshlrev_b64 v[2:3], 2, v[66:67]
	v_lshl_add_u64 v[88:89], s[14:15], 0, v[2:3]
	v_lshl_add_u64 v[90:91], s[56:57], 0, v[2:3]
	v_lshl_add_u64 v[92:93], s[12:13], 0, v[2:3]
	v_lshl_add_u64 v[94:95], s[18:19], 0, v[2:3]
	v_lshl_add_u64 v[96:97], s[16:17], 0, v[2:3]
	v_mul_u32_u24_e32 v2, 0x5556, v0
	v_mov_b32_e32 v3, -3
	s_movk_i32 s18, 0x1a0
	v_mul_i32_i24_sdwa v3, v2, v3 dst_sel:DWORD dst_unused:UNUSED_PAD src0_sel:WORD_1 src1_sel:DWORD
	v_mul_u32_u24_sdwa v19, v2, s18 dst_sel:DWORD dst_unused:UNUSED_PAD src0_sel:WORD_1 src1_sel:DWORD
	v_mul_u32_u24_e32 v2, 0xa3e, v0
	v_lshrrev_b32_e32 v2, 12, v2
	v_mad_i32_i24 v112, v10, s4, v5
	v_mad_i32_i24 v113, v11, s4, v6
	v_mad_i32_i24 v114, v12, s4, v7
	v_mad_i32_i24 v115, v14, s4, v8
	v_add_lshl_u32 v20, v3, v0, 4
	v_mul_u32_u24_e32 v3, 0xa3e, v5
	v_mul_u32_u24_e32 v5, 0xa3e, v6
	v_mul_u32_u24_e32 v6, 0xa3e, v7
	v_mul_u32_u24_e32 v7, 0xa3e, v8
	v_and_b32_e32 v2, 0x1f0, v2
	v_lshlrev_b32_e32 v8, 4, v0
	v_add_u32_e32 v123, v2, v8
	v_lshrrev_b32_e32 v2, 12, v3
	v_and_b32_e32 v2, 0x3f0, v2
	v_add_u32_e32 v124, v2, v8
	v_lshrrev_b32_e32 v2, 12, v5
	v_and_b32_e32 v2, 0x7f0, v2
	v_add_u32_e32 v125, v2, v8
	v_lshrrev_b32_e32 v2, 12, v6
	v_and_b32_e32 v2, 0x7f0, v2
	v_mul_u32_u24_e32 v1, 0x2fb, v0
	v_add_u32_e32 v126, v2, v8
	v_lshrrev_b32_e32 v2, 12, v7
	v_and_b32_e32 v4, 63, v0
	v_lshrrev_b32_e32 v9, 16, v1
	v_and_b32_e32 v2, 0x7f0, v2
	v_mad_i32_i24 v1, v9, s4, v0
	v_and_b32_e32 v18, 15, v0
	v_add_u32_e32 v127, v2, v8
	v_lshrrev_b32_e32 v2, 2, v0
	s_movk_i32 s19, 0x70
	v_and_b32_e32 v98, 48, v0
	v_lshlrev_b32_e32 v66, 4, v4
	v_mov_b32_e32 v99, v67
	v_mov_b32_e32 v4, 0xfffff920
	v_and_or_b32 v128, v2, s19, v18
	v_lshl_add_u64 v[102:103], s[20:21], 0, v[98:99]
	v_mad_u64_u32 v[2:3], s[20:21], s2, 22, v[0:1]
	v_mov_b32_e32 v5, -1
	v_mad_u64_u32 v[104:105], s[20:21], v2, 5, v[4:5]
	v_min_u32_e32 v13, 21, v12
	v_min_u32_e32 v15, 21, v14
	v_min_u32_e32 v17, 21, v16
	s_movk_i32 s20, 0x410
	v_mov_b32_e32 v2, 0xfffa6a00
	v_mad_u32_u24 v99, v17, s20, v2
	v_mad_u32_u24 v105, v15, s20, v2
	v_mad_u32_u24 v130, v13, s20, v2
	v_mad_u32_u24 v131, v11, s20, v2
	v_mad_u32_u24 v132, v10, s20, v2
	v_mad_u32_u24 v133, v9, s20, v2
	v_lshlrev_b32_e32 v2, 6, v0
	s_mul_i32 s20, s2, 0x42000
	v_and_b32_e32 v2, 0x7000, v2
	v_add_u32_e32 v2, s20, v2
	v_lshlrev_b32_e32 v3, 8, v18
	v_lshlrev_b32_e32 v68, 2, v0
	v_mov_b32_e32 v69, v67
	s_movk_i32 s6, 0xb0
	s_movk_i32 s10, 0x102
	v_mul_lo_u32 v21, v1, s18
	v_lshlrev_b32_e32 v22, 4, v9
	v_mul_lo_u32 v23, v112, s18
	v_lshlrev_b32_e32 v24, 4, v10
	v_mul_lo_u32 v25, v113, s18
	v_lshlrev_b32_e32 v26, 4, v11
	s_movk_i32 s12, 0x3a4
	v_mul_lo_u32 v27, v114, s18
	v_lshlrev_b32_e32 v12, 4, v12
	s_movk_i32 s14, 0x264
	v_mul_lo_u32 v28, v115, s18
	v_lshlrev_b32_e32 v14, 4, v14
	s_movk_i32 s16, 0x124
	v_mul_lo_u32 v29, v116, s18
	v_lshlrev_b32_e32 v16, 4, v16
	v_mul_u32_u24_e32 v6, 0x1a0, v128
	v_or3_b32 v2, v2, v3, v98
	v_lshlrev_b32_e32 v106, 4, v0
	v_cmp_gt_u32_e64 s[22:23], 22, v0
	v_cmp_gt_u32_e64 s[4:5], 11, v0
	v_lshl_add_u64 v[70:71], s[42:43], 0, v[68:69]
	v_lshl_add_u64 v[74:75], s[46:47], 0, v[68:69]
	v_cmp_gt_u32_e64 s[6:7], s6, v0
	v_lshl_add_u64 v[78:79], s[50:51], 0, v[68:69]
	v_lshl_add_u64 v[80:81], s[28:29], 0, v[68:69]
	v_lshl_add_u64 v[82:83], s[48:49], 0, v[68:69]
	v_lshl_add_u64 v[84:85], s[26:27], 0, v[68:69]
	v_lshl_add_u64 v[86:87], s[24:25], 0, v[68:69]
	v_cmp_gt_u32_e64 s[10:11], s10, v0
	v_lshlrev_b32_e32 v69, 5, v9
	v_lshlrev_b32_e32 v118, 5, v10
	v_lshlrev_b32_e32 v119, 5, v11
	v_cmp_gt_u32_e64 s[12:13], s12, v0
	v_lshlrev_b32_e32 v120, 5, v13
	v_cmp_gt_u32_e64 s[14:15], s14, v0
	v_lshlrev_b32_e32 v121, 5, v15
	v_cmp_gt_u32_e64 s[16:17], s16, v0
	v_lshlrev_b32_e32 v122, 5, v17
	v_mad_u32_u24 v129, v18, s18, v98
	s_mov_b32 s27, 0x20000
	s_mov_b32 s26, 0x1080000
	s_and_b32 s25, s53, 0xffff
	s_mov_b32 s24, s52
	v_lshl_add_u64 v[100:101], s[58:59], 0, v[66:67]
	v_cmp_eq_u32_e64 s[18:19], 0, v0
	s_mul_i32 s29, s2, 0x5960
	s_movk_i32 s33, 0x7000
	v_add_u32_e32 v134, 0xffbe0000, v2
	v_mov_b32_e32 v108, v106
	v_mov_b32_e32 v109, v67
	s_movk_i32 s35, 0x1000
	s_movk_i32 s41, 0x2000
	s_movk_i32 s43, 0x3000
	s_movk_i32 s45, 0x5000
	s_movk_i32 s47, 0x6000
	s_mov_b32 s49, 0x8000
	s_mov_b32 s60, 0xa000
	s_mov_b32 s61, 0xb000
	s_mov_b32 s28, 0x3f3504f3
	s_mov_b32 s62, 0x378e98ab
	s_mov_b32 s63, 0x3b7cd369
	s_mov_b32 s64, 0xbcc618b2
	s_mov_b32 s65, 0x3dda74e4
	s_mov_b32 s66, 0x3f228afd
	s_mov_b32 s67, 0x3e03c728
	s_mov_b32 s68, 0xbfb8aa3b
	s_mov_b32 s69, 0x42ce8ed0
	s_mov_b32 s70, 0xc2b17218
	v_mov_b32_e32 v135, 0x3ba10414
	s_brev_b32 s71, -2
	s_mov_b32 s72, 0xf800000
	v_mov_b32_e32 v136, 0x260
	v_add_u32_e32 v137, v19, v20
	s_movk_i32 s73, 0x401
	s_mov_b32 s74, 0x3ea7ba05
	s_mov_b32 s34, 0xbfba00e3
	s_mov_b32 s40, 0x3f87dc22
	s_mov_b32 s42, 0x3fb5f0e3
	v_add_u32_e32 v138, v21, v22
	v_add_u32_e32 v139, v23, v24
	v_add_u32_e32 v140, v25, v26
	v_add_u32_e32 v141, v27, v12
	v_add_u32_e32 v142, v28, v14
	v_add_u32_e32 v143, v29, v16
	v_add_u32_e32 v144, v98, v6
	s_mov_b32 s75, 0x12000
	s_mov_b32 s76, 0x14000
	s_mov_b32 s77, 0x15000
	s_mov_b32 s78, 0x16000
	s_mov_b32 s79, 0x17000
	s_mov_b32 s80, 0x19000
	s_mov_b32 s81, 0x1a000
	s_mov_b32 s82, 0x1b000
	s_mov_b32 s83, 0x1c000
	s_mov_b32 s84, 0x1e000
	s_mov_b32 s85, 0x1f000
	s_mov_b32 s86, 0x21000
	s_mov_b32 s87, 0x23000
	s_mov_b32 s88, 0x24000
	s_mov_b32 s89, 0x25000
	s_mov_b32 s90, 0x26000
	s_mov_b32 s91, 0x28000
	s_mov_b32 s92, 0x29000
	s_mov_b32 s93, 0x2a000
	v_mov_b32_e32 v145, 1
	v_mov_b32_e32 v146, 0xb9c68948
	v_mov_b32_e32 v147, 0x7f800000
	v_mov_b32_e32 v148, v67
	v_mov_b32_e32 v149, v67
	v_mov_b32_e32 v150, v67
	v_mov_b32_e32 v151, v67
	s_mov_b32 s44, 0xbe91a98e
	s_mov_b32 s46, 0x3e827906
	s_mov_b32 s48, 0x4038aa3b
	s_mov_b64 s[98:99], exec
	s_and_b64 exec, s[98:99], s[4:5]
	global_load_dword v244, v[70:71], off
	global_load_dword v245, v[72:73], off
	global_load_dword v246, v[72:73], off offset:64
	s_and_b64 exec, s[98:99], s[22:23]
	global_load_dword v247, v[76:77], off
	global_load_dword v248, v[74:75], off
	s_and_b64 exec, s[98:99], s[6:7]
	global_load_dword v249, v[80:81], off
	global_load_dword v250, v[78:79], off
	global_load_dword v251, v[82:83], off
	global_load_dword v252, v[84:85], off
	global_load_dword v253, v[86:87], off
	s_and_b64 exec, s[98:99], s[22:23]
	v_mov_b32_e32 v254, v104
	v_ashrrev_i32_e32 v255, 31, v104
	v_lshl_add_u64 v[254:255], v[254:255], 2, s[38:39]
	global_load_dword v244, v[254:255], off
	global_load_dword v245, v[254:255], off offset:16
	s_and_b64 exec, s[98:99], s[8:9]
	global_load_dword v246, v[90:91], off
	global_load_dword v247, v[88:89], off
	global_load_dword v248, v[92:93], off
	global_load_dword v249, v[94:95], off
	global_load_dword v250, v[96:97], off
	s_mov_b64 exec, s[98:99]
	s_branch .LBB3_4
